# cfgJ + expert 2 split by matrix in REC: bx>=230 WGs convert gate/up matrices, the 16 S5-scan WGs convert the down matrix after their scan
# speedup vs baseline: 1.0072x; 1.0072x over previous
.LBB0_8:
	s_and_saveexec_b64 s[12:13], vcc
	s_cbranch_execz .LBB0_7
	s_mul_hi_u32 s17, s8, 0xe00000
	s_mul_i32 s16, s8, 0xe00000
	s_mul_hi_u32 s15, s8, 0x3800
	s_mul_i32 s14, s8, 0x3800
	v_lshl_add_u64 v[28:29], s[16:17], 2, v[22:23]
	s_lshl_b32 s67, s3, 7
	s_mov_b64 s[18:19], 0
	v_mov_b32_e32 v32, v74
	v_mov_b32_e32 v30, v1
	v_mov_b32_e32 v33, v69
	s_cmp_eq_u32 s99, 3
	s_cbranch_scc0 .Lnsk10
	v_add_u32_e32 v71, 0x35a0, v40
	v_add_u32_e32 v73, 0x35a8, v40
	v_add_u32_e32 v76, 0x39c0, v40
	v_add_u32_e32 v77, 0x39c8, v40
	v_add_u32_e32 v82, 0x3de0, v40
	v_add_u32_e32 v83, 0x3de8, v40
	v_add_u32_e32 v84, 0x400, v75
	v_add_u32_e32 v85, 0x600, v75
	s_mov_b64 exec, 0
.Lnsk10:
.LBB0_10:
	v_ashrrev_i32_e32 v34, 31, v33
	v_lshrrev_b32_e32 v34, 28, v34
	v_add_u32_e32 v34, v33, v34
	v_ashrrev_i32_e32 v37, 4, v34
	v_lshlrev_b32_e32 v36, 5, v37
	v_mad_u64_u32 v[38:39], s[0:1], v37, s25, v[30:31]
	v_lshlrev_b32_e32 v86, 11, v37
	v_ashrrev_i32_e32 v37, 31, v36
	v_ashrrev_i32_e32 v39, 31, v38
	v_sub_u32_e32 v86, v32, v86
	v_lshl_add_u64 v[88:89], v[36:37], 2, v[28:29]
	v_ashrrev_i32_e32 v87, 31, v86
	v_lshl_add_u64 v[38:39], v[38:39], 2, v[88:89]
	v_lshl_add_u64 v[148:149], v[18:19], 0, v[86:87]
	v_add_co_u32_e64 v86, s[0:1], s26, v38
	v_ashrrev_i32_e32 v34, 6, v34
	s_nop 0
	v_addc_co_u32_e64 v87, s[0:1], 0, v39, s[0:1]
	v_add_co_u32_e64 v90, s[0:1], s27, v38
	v_ashrrev_i32_e32 v35, 31, v34
	s_nop 0
	v_addc_co_u32_e64 v91, s[0:1], 0, v39, s[0:1]
	v_add_co_u32_e64 v94, s[0:1], s28, v38
	v_lshlrev_b64 v[34:35], 8, v[34:35]
	s_nop 0
	v_addc_co_u32_e64 v95, s[0:1], 0, v39, s[0:1]
	v_add_co_u32_e64 v98, s[0:1], s22, v38
	v_lshl_add_u64 v[146:147], v[34:35], 0, s[14:15]
	s_nop 0
	v_addc_co_u32_e64 v99, s[0:1], 0, v39, s[0:1]
	v_add_co_u32_e64 v102, s[0:1], s29, v38
	v_and_or_b32 v154, v36, s24, v146
	s_nop 0
	v_addc_co_u32_e64 v103, s[0:1], 0, v39, s[0:1]
	v_add_co_u32_e64 v106, s[0:1], s30, v38
	global_load_dwordx4 v[34:37], v[38:39], off nt
	s_nop 0
	v_addc_co_u32_e64 v107, s[0:1], 0, v39, s[0:1]
	v_add_co_u32_e64 v110, s[0:1], s31, v38
	v_add_u32_e32 v71, 0x35a0, v40
	s_nop 0
	v_addc_co_u32_e64 v111, s[0:1], 0, v39, s[0:1]
	v_add_co_u32_e64 v114, s[0:1], s33, v38
	v_add_u32_e32 v73, 0x35a8, v40
	s_nop 0
	v_addc_co_u32_e64 v115, s[0:1], 0, v39, s[0:1]
	v_add_co_u32_e64 v118, s[0:1], s34, v38
	v_add_u32_e32 v76, 0x39c0, v40
	s_nop 0
	v_addc_co_u32_e64 v119, s[0:1], 0, v39, s[0:1]
	v_add_co_u32_e64 v122, s[0:1], s35, v38
	v_add_u32_e32 v77, 0x39c8, v40
	s_nop 0
	v_addc_co_u32_e64 v123, s[0:1], 0, v39, s[0:1]
	v_add_co_u32_e64 v126, s[0:1], s60, v38
	v_add_u32_e32 v82, 0x3de0, v40
	s_nop 0
	v_addc_co_u32_e64 v127, s[0:1], 0, v39, s[0:1]
	v_add_co_u32_e64 v130, s[0:1], s61, v38
	v_add_u32_e32 v83, 0x3de8, v40
	s_nop 0
	v_addc_co_u32_e64 v131, s[0:1], 0, v39, s[0:1]
	v_add_co_u32_e64 v134, s[0:1], s62, v38
	v_add_u32_e32 v84, 0x400, v75
	s_nop 0
	v_addc_co_u32_e64 v135, s[0:1], 0, v39, s[0:1]
	v_add_co_u32_e64 v138, s[0:1], s63, v38
	v_add_u32_e32 v85, 0x600, v75
	s_nop 0
	v_addc_co_u32_e64 v139, s[0:1], 0, v39, s[0:1]
	v_add_co_u32_e64 v38, s[0:1], s64, v38
	v_mov_b32_e32 v2, 0
	s_nop 0
	v_addc_co_u32_e64 v39, s[0:1], 0, v39, s[0:1]
	global_load_dwordx4 v[86:89], v[86:87], off nt
	s_nop 0
	global_load_dwordx4 v[90:93], v[90:91], off nt
	s_nop 0
	global_load_dwordx4 v[94:97], v[94:95], off nt
	s_nop 0
	global_load_dwordx4 v[98:101], v[98:99], off nt
	s_nop 0
	global_load_dwordx4 v[102:105], v[102:103], off nt
	s_nop 0
	global_load_dwordx4 v[106:109], v[106:107], off nt
	s_nop 0
	global_load_dwordx4 v[110:113], v[110:111], off nt
	s_nop 0
	global_load_dwordx4 v[114:117], v[114:115], off nt
	s_nop 0
	global_load_dwordx4 v[118:121], v[118:119], off nt
	s_nop 0
	global_load_dwordx4 v[122:125], v[122:123], off nt
	s_nop 0
	global_load_dwordx4 v[126:129], v[126:127], off nt
	s_nop 0
	global_load_dwordx4 v[130:133], v[130:131], off nt
	s_nop 0
	global_load_dwordx4 v[134:137], v[134:135], off nt
	s_nop 0
	global_load_dwordx4 v[138:141], v[138:139], off nt
	s_nop 0
	global_load_dwordx4 v[142:145], v[38:39], off nt
	v_mov_b32_e32 v3, 0
	v_mov_b32_e32 v4, 0
	v_mov_b32_e32 v5, 0
	v_mov_b32_e32 v6, 0
	v_mov_b32_e32 v7, 0
	v_mov_b32_e32 v8, 0
	v_mov_b32_e32 v9, 0
	v_mov_b32_e32 v10, 0
	v_mov_b32_e32 v11, 0
	v_mov_b32_e32 v12, 0
	v_mov_b32_e32 v13, 0
	v_mov_b32_e32 v14, 0
	v_mov_b32_e32 v15, 0
	v_mov_b32_e32 v16, 0
	v_mov_b32_e32 v17, 0
	v_or_b32_e32 v146, v154, v66
	v_lshlrev_b64 v[38:39], 11, v[146:147]
	v_or_b32_e32 v146, v154, v68
	v_lshlrev_b64 v[150:151], 11, v[146:147]
	v_or_b32_e32 v146, v154, v70
	v_lshlrev_b64 v[152:153], 11, v[146:147]
	v_or_b32_e32 v146, v154, v72
	v_lshl_add_u64 v[38:39], v[148:149], 0, v[38:39]
	v_lshlrev_b64 v[146:147], 11, v[146:147]
	v_lshl_add_u64 v[150:151], v[148:149], 0, v[150:151]
	v_lshl_add_u64 v[152:153], v[148:149], 0, v[152:153]
	s_waitcnt vmcnt(15)
	ds_write2_b32 v40, v34, v35 offset1:1
	ds_write2_b32 v40, v36, v37 offset0:2 offset1:3
	s_waitcnt vmcnt(14)
	ds_write2_b32 v41, v86, v87 offset1:1
	ds_write2_b32 v42, v88, v89 offset1:1
	s_waitcnt vmcnt(13)
	ds_write2_b32 v43, v90, v91 offset1:1
	ds_write2_b32 v44, v92, v93 offset1:1
	s_waitcnt vmcnt(12)
	ds_write2_b32 v45, v94, v95 offset1:1
	ds_write2_b32 v46, v96, v97 offset1:1
	s_waitcnt vmcnt(11)
	ds_write2_b32 v47, v98, v99 offset1:1
	ds_write2_b32 v48, v100, v101 offset1:1
	s_waitcnt vmcnt(10)
	ds_write2_b32 v49, v102, v103 offset1:1
	ds_write2_b32 v50, v104, v105 offset1:1
	s_waitcnt vmcnt(9)
	ds_write2_b32 v51, v106, v107 offset1:1
	ds_write2_b32 v52, v108, v109 offset1:1
	s_waitcnt vmcnt(8)
	ds_write2_b32 v53, v110, v111 offset1:1
	ds_write2_b32 v54, v112, v113 offset1:1
	s_waitcnt vmcnt(7)
	ds_write2_b32 v55, v114, v115 offset1:1
	ds_write2_b32 v56, v116, v117 offset1:1
	s_waitcnt vmcnt(6)
	ds_write2_b32 v57, v118, v119 offset1:1
	ds_write2_b32 v58, v120, v121 offset1:1
	s_waitcnt vmcnt(5)
	ds_write2_b32 v59, v122, v123 offset1:1
	ds_write2_b32 v60, v124, v125 offset1:1
	s_waitcnt vmcnt(4)
	ds_write2_b32 v61, v126, v127 offset1:1
	ds_write2_b32 v62, v128, v129 offset1:1
	s_waitcnt vmcnt(3)
	ds_write2_b32 v63, v130, v131 offset1:1
	ds_write2_b32 v64, v132, v133 offset1:1
	s_waitcnt vmcnt(2)
	ds_write2_b32 v71, v134, v135 offset1:1
	ds_write2_b32 v73, v136, v137 offset1:1
	s_waitcnt vmcnt(1)
	ds_write2_b32 v76, v138, v139 offset1:1
	ds_write2_b32 v77, v140, v141 offset1:1
	s_waitcnt vmcnt(0)
	ds_write2_b32 v82, v142, v143 offset1:1
	ds_write2_b32 v83, v144, v145 offset1:1
	s_waitcnt lgkmcnt(0)
	ds_read2_b32 v[34:35], v75 offset1:8
	ds_read2_b32 v[36:37], v75 offset0:33 offset1:41
	ds_read2_b32 v[86:87], v75 offset0:132 offset1:140
	ds_read2_b32 v[88:89], v75 offset0:165 offset1:173
	ds_read2_b32 v[90:91], v84 offset0:8 offset1:16
	ds_read2_b32 v[92:93], v84 offset0:41 offset1:49
	ds_read2_b32 v[94:95], v84 offset0:140 offset1:148
	ds_read2_b32 v[96:97], v84 offset0:173 offset1:181
	ds_read2_b32 v[98:99], v75 offset0:66 offset1:74
	ds_read2_b32 v[100:101], v75 offset0:99 offset1:107
	ds_read2_b32 v[102:103], v75 offset0:198 offset1:206
	ds_read2_b32 v[104:105], v75 offset0:231 offset1:239
	ds_read2_b32 v[106:107], v84 offset0:74 offset1:82
	ds_read2_b32 v[108:109], v84 offset0:107 offset1:115
	ds_read2_b32 v[110:111], v84 offset0:206 offset1:214
	ds_read2_b32 v[112:113], v84 offset0:239 offset1:247
	ds_read2_b32 v[114:115], v75 offset0:16 offset1:24
	ds_read2_b32 v[116:117], v75 offset0:49 offset1:57
	ds_read2_b32 v[118:119], v75 offset0:148 offset1:156
	ds_read2_b32 v[120:121], v75 offset0:181 offset1:189
	ds_read2_b32 v[122:123], v84 offset0:24 offset1:32
	ds_read2_b32 v[124:125], v84 offset0:57 offset1:65
	ds_read2_b32 v[126:127], v84 offset0:156 offset1:164
	ds_read2_b32 v[128:129], v84 offset0:189 offset1:197
	ds_read2_b32 v[130:131], v75 offset0:82 offset1:90
	ds_read2_b32 v[132:133], v75 offset0:115 offset1:123
	ds_read2_b32 v[134:135], v75 offset0:214 offset1:222
	ds_read2_b32 v[136:137], v75 offset0:247 offset1:255
	ds_read2_b32 v[138:139], v84 offset0:90 offset1:98
	ds_read2_b32 v[140:141], v84 offset0:123 offset1:131
	ds_read2_b32 v[142:143], v84 offset0:222 offset1:230
	ds_read2_b32 v[144:145], v85 offset0:127 offset1:135
	s_waitcnt lgkmcnt(14)
	v_mul_f32_e32 v34, 0x43800000, v34
	v_mul_f32_e32 v36, 0x43800000, v36
	v_mul_f32_e32 v86, 0x43800000, v86
	v_mul_f32_e32 v88, 0x43800000, v88
	v_mul_f32_e32 v90, 0x43800000, v90
	v_mul_f32_e32 v92, 0x43800000, v92
	v_mul_f32_e32 v94, 0x43800000, v94
	v_mul_f32_e32 v96, 0x43800000, v96
	v_mul_f32_e32 v35, 0x43800000, v35
	v_mul_f32_e32 v37, 0x43800000, v37
	v_mul_f32_e32 v87, 0x43800000, v87
	v_mul_f32_e32 v89, 0x43800000, v89
	v_mul_f32_e32 v91, 0x43800000, v91
	v_mul_f32_e32 v93, 0x43800000, v93
	v_mul_f32_e32 v95, 0x43800000, v95
	v_mul_f32_e32 v97, 0x43800000, v97
	v_med3_f32 v34, v34, s65, v65
	v_med3_f32 v36, v36, s65, v65
	v_med3_f32 v86, v86, s65, v65
	v_med3_f32 v88, v88, s65, v65
	v_med3_f32 v90, v90, s65, v65
	v_med3_f32 v92, v92, s65, v65
	v_med3_f32 v94, v94, s65, v65
	v_med3_f32 v96, v96, s65, v65
	v_mul_f32_e32 v114, 0x43800000, v114
	v_mul_f32_e32 v116, 0x43800000, v116
	s_waitcnt lgkmcnt(13)
	v_mul_f32_e32 v118, 0x43800000, v118
	s_waitcnt lgkmcnt(12)
	v_mul_f32_e32 v120, 0x43800000, v120
	s_waitcnt lgkmcnt(11)
	v_mul_f32_e32 v122, 0x43800000, v122
	s_waitcnt lgkmcnt(10)
	v_mul_f32_e32 v124, 0x43800000, v124
	s_waitcnt lgkmcnt(9)
	v_mul_f32_e32 v126, 0x43800000, v126
	s_waitcnt lgkmcnt(8)
	v_mul_f32_e32 v128, 0x43800000, v128
	v_med3_f32 v35, v35, s65, v65
	v_med3_f32 v37, v37, s65, v65
	v_med3_f32 v87, v87, s65, v65
	v_med3_f32 v89, v89, s65, v65
	v_med3_f32 v91, v91, s65, v65
	v_med3_f32 v93, v93, s65, v65
	v_med3_f32 v95, v95, s65, v65
	v_med3_f32 v97, v97, s65, v65
	v_cvt_pk_fp8_f32 v2, v34, v36
	v_cvt_pk_fp8_f32 v3, v86, v88
	v_cvt_pk_fp8_f32 v4, v90, v92
	v_cvt_pk_fp8_f32 v5, v94, v96
	v_mul_f32_e32 v115, 0x43800000, v115
	v_mul_f32_e32 v117, 0x43800000, v117
	v_mul_f32_e32 v119, 0x43800000, v119
	v_mul_f32_e32 v121, 0x43800000, v121
	v_mul_f32_e32 v123, 0x43800000, v123
	v_mul_f32_e32 v125, 0x43800000, v125
	v_mul_f32_e32 v127, 0x43800000, v127
	v_mul_f32_e32 v129, 0x43800000, v129
	v_med3_f32 v114, v114, s65, v65
	v_med3_f32 v116, v116, s65, v65
	v_med3_f32 v118, v118, s65, v65
	v_med3_f32 v120, v120, s65, v65
	v_med3_f32 v122, v122, s65, v65
	v_med3_f32 v124, v124, s65, v65
	v_med3_f32 v126, v126, s65, v65
	v_med3_f32 v128, v128, s65, v65
	v_cvt_pk_fp8_f32 v6, v35, v37
	v_cvt_pk_fp8_f32 v7, v87, v89
	v_cvt_pk_fp8_f32 v8, v91, v93
	v_cvt_pk_fp8_f32 v9, v95, v97
	v_mul_f32_e32 v98, 0x43800000, v98
	v_mul_f32_e32 v100, 0x43800000, v100
	v_mul_f32_e32 v102, 0x43800000, v102
	v_mul_f32_e32 v104, 0x43800000, v104
	v_mul_f32_e32 v106, 0x43800000, v106
	v_mul_f32_e32 v108, 0x43800000, v108
	v_mul_f32_e32 v110, 0x43800000, v110
	v_mul_f32_e32 v112, 0x43800000, v112
	v_med3_f32 v115, v115, s65, v65
	v_med3_f32 v117, v117, s65, v65
	v_med3_f32 v119, v119, s65, v65
	v_med3_f32 v121, v121, s65, v65
	v_med3_f32 v123, v123, s65, v65
	v_med3_f32 v125, v125, s65, v65
	v_med3_f32 v127, v127, s65, v65
	v_med3_f32 v129, v129, s65, v65
	v_cvt_pk_fp8_f32 v10, v114, v116
	v_cvt_pk_fp8_f32 v11, v118, v120
	v_cvt_pk_fp8_f32 v12, v122, v124
	v_cvt_pk_fp8_f32 v13, v126, v128
	v_mul_f32_e32 v99, 0x43800000, v99
	v_mul_f32_e32 v101, 0x43800000, v101
	v_mul_f32_e32 v103, 0x43800000, v103
	v_mul_f32_e32 v105, 0x43800000, v105
	v_mul_f32_e32 v107, 0x43800000, v107
	v_mul_f32_e32 v109, 0x43800000, v109
	v_mul_f32_e32 v111, 0x43800000, v111
	v_mul_f32_e32 v113, 0x43800000, v113
	v_med3_f32 v98, v98, s65, v65
	v_med3_f32 v100, v100, s65, v65
	v_med3_f32 v102, v102, s65, v65
	v_med3_f32 v104, v104, s65, v65
	v_med3_f32 v106, v106, s65, v65
	v_med3_f32 v108, v108, s65, v65
	v_med3_f32 v110, v110, s65, v65
	v_med3_f32 v112, v112, s65, v65
	v_cvt_pk_fp8_f32 v14, v115, v117
	v_cvt_pk_fp8_f32 v15, v119, v121
	v_cvt_pk_fp8_f32 v16, v123, v125
	v_cvt_pk_fp8_f32 v17, v127, v129
	s_waitcnt lgkmcnt(7)
	v_mul_f32_e32 v130, 0x43800000, v130
	s_waitcnt lgkmcnt(6)
	v_mul_f32_e32 v132, 0x43800000, v132
	s_waitcnt lgkmcnt(5)
	v_mul_f32_e32 v134, 0x43800000, v134
	s_waitcnt lgkmcnt(4)
	v_mul_f32_e32 v136, 0x43800000, v136
	s_waitcnt lgkmcnt(3)
	v_mul_f32_e32 v138, 0x43800000, v138
	s_waitcnt lgkmcnt(2)
	v_mul_f32_e32 v140, 0x43800000, v140
	s_waitcnt lgkmcnt(1)
	v_mul_f32_e32 v142, 0x43800000, v142
	s_waitcnt lgkmcnt(0)
	v_mul_f32_e32 v144, 0x43800000, v144
	v_med3_f32 v99, v99, s65, v65
	v_med3_f32 v101, v101, s65, v65
	v_med3_f32 v103, v103, s65, v65
	v_med3_f32 v105, v105, s65, v65
	v_med3_f32 v107, v107, s65, v65
	v_med3_f32 v109, v109, s65, v65
	v_med3_f32 v111, v111, s65, v65
	v_med3_f32 v113, v113, s65, v65
	v_cvt_pk_fp8_f32 v2, v98, v100 op_sel:[0,0,1]
	v_cvt_pk_fp8_f32 v3, v102, v104 op_sel:[0,0,1]
	v_cvt_pk_fp8_f32 v4, v106, v108 op_sel:[0,0,1]
	v_cvt_pk_fp8_f32 v5, v110, v112 op_sel:[0,0,1]
	v_mul_f32_e32 v131, 0x43800000, v131
	v_mul_f32_e32 v133, 0x43800000, v133
	v_mul_f32_e32 v135, 0x43800000, v135
	v_mul_f32_e32 v137, 0x43800000, v137
	v_mul_f32_e32 v139, 0x43800000, v139
	v_mul_f32_e32 v141, 0x43800000, v141
	v_mul_f32_e32 v143, 0x43800000, v143
	v_mul_f32_e32 v145, 0x43800000, v145
	v_med3_f32 v130, v130, s65, v65
	v_med3_f32 v132, v132, s65, v65
	v_med3_f32 v134, v134, s65, v65
	v_med3_f32 v136, v136, s65, v65
	v_med3_f32 v138, v138, s65, v65
	v_med3_f32 v140, v140, s65, v65
	v_med3_f32 v142, v142, s65, v65
	v_med3_f32 v144, v144, s65, v65
	v_cvt_pk_fp8_f32 v6, v99, v101 op_sel:[0,0,1]
	v_cvt_pk_fp8_f32 v7, v103, v105 op_sel:[0,0,1]
	v_cvt_pk_fp8_f32 v8, v107, v109 op_sel:[0,0,1]
	v_cvt_pk_fp8_f32 v9, v111, v113 op_sel:[0,0,1]
	v_med3_f32 v131, v131, s65, v65
	v_med3_f32 v133, v133, s65, v65
	v_med3_f32 v135, v135, s65, v65
	v_med3_f32 v137, v137, s65, v65
	v_med3_f32 v139, v139, s65, v65
	v_med3_f32 v141, v141, s65, v65
	v_med3_f32 v143, v143, s65, v65
	v_med3_f32 v145, v145, s65, v65
	v_cvt_pk_fp8_f32 v10, v130, v132 op_sel:[0,0,1]
	v_cvt_pk_fp8_f32 v11, v134, v136 op_sel:[0,0,1]
	v_cvt_pk_fp8_f32 v12, v138, v140 op_sel:[0,0,1]
	v_cvt_pk_fp8_f32 v13, v142, v144 op_sel:[0,0,1]
	v_cvt_pk_fp8_f32 v14, v131, v133 op_sel:[0,0,1]
	v_cvt_pk_fp8_f32 v15, v135, v137 op_sel:[0,0,1]
	v_cvt_pk_fp8_f32 v16, v139, v141 op_sel:[0,0,1]
	v_cvt_pk_fp8_f32 v17, v143, v145 op_sel:[0,0,1]
	v_lshl_add_u64 v[146:147], v[148:149], 0, v[146:147]
	global_store_dwordx4 v[38:39], v[2:5], off nt
	global_store_dwordx4 v[150:151], v[6:9], off nt
	global_store_dwordx4 v[152:153], v[10:13], off nt
	global_store_dwordx4 v[146:147], v[14:17], off nt
	v_add_u32_e32 v33, s3, v33
	s_waitcnt lgkmcnt(0)
	v_cmp_lt_i32_e64 s[6:7], s66, v33
	v_add_u32_e32 v30, s23, v30
	s_or_b64 s[18:19], s[6:7], s[18:19]
	v_add_u32_e32 v32, s67, v32
	s_andn2_b64 exec, exec, s[18:19]
	s_cbranch_execnz .LBB0_10
	s_or_b64 exec, exec, s[18:19]
	s_mov_b64 exec, -1
	s_bitset1_b32 s14, 7
	v_lshl_add_u64 v[28:29], s[16:17], 2, v[24:25]
	s_mov_b64 s[16:17], 0
	v_mov_b32_e32 v86, v74
	v_mov_b32_e32 v30, v1
	v_mov_b32_e32 v87, v69
	s_cmp_eq_u32 s99, 3
	s_cbranch_scc0 .Lnsk12
	s_mov_b64 exec, 0
.Lnsk12:
.LBB0_12:
	v_ashrrev_i32_e32 v32, 31, v87
	v_lshrrev_b32_e32 v32, 28, v32
	v_add_u32_e32 v32, v87, v32
	v_ashrrev_i32_e32 v33, 4, v32
	v_ashrrev_i32_e32 v32, 6, v32
	v_lshlrev_b32_e32 v34, 5, v33
	v_mad_u64_u32 v[36:37], s[0:1], v33, s25, v[30:31]
	v_lshlrev_b32_e32 v38, 11, v33
	v_ashrrev_i32_e32 v33, 31, v32
	v_ashrrev_i32_e32 v35, 31, v34
	v_ashrrev_i32_e32 v37, 31, v36
	v_lshlrev_b64 v[32:33], 8, v[32:33]
	v_lshl_add_u64 v[88:89], v[34:35], 2, v[28:29]
	v_lshl_add_u64 v[152:153], s[14:15], 0, v[32:33]
	v_lshl_add_u64 v[32:33], v[36:37], 2, v[88:89]
	v_and_or_b32 v154, v34, s24, v152
	v_add_co_u32_e64 v34, s[0:1], s26, v32
	global_load_dwordx4 v[88:91], v[32:33], off nt
	s_nop 0
	v_addc_co_u32_e64 v35, s[0:1], 0, v33, s[0:1]
	v_add_co_u32_e64 v36, s[0:1], s27, v32
	v_mov_b32_e32 v2, 0
	s_nop 0
	v_addc_co_u32_e64 v37, s[0:1], 0, v33, s[0:1]
	v_add_co_u32_e64 v100, s[0:1], s28, v32
	v_mov_b32_e32 v3, 0
	s_nop 0
	v_addc_co_u32_e64 v101, s[0:1], 0, v33, s[0:1]
	v_add_co_u32_e64 v104, s[0:1], s22, v32
	v_mov_b32_e32 v4, 0
	s_nop 0
	v_addc_co_u32_e64 v105, s[0:1], 0, v33, s[0:1]
	v_add_co_u32_e64 v108, s[0:1], s29, v32
	v_mov_b32_e32 v5, 0
	s_nop 0
	v_addc_co_u32_e64 v109, s[0:1], 0, v33, s[0:1]
	v_add_co_u32_e64 v112, s[0:1], s30, v32
	v_mov_b32_e32 v6, 0
	s_nop 0
	v_addc_co_u32_e64 v113, s[0:1], 0, v33, s[0:1]
	v_add_co_u32_e64 v116, s[0:1], s31, v32
	v_mov_b32_e32 v7, 0
	s_nop 0
	v_addc_co_u32_e64 v117, s[0:1], 0, v33, s[0:1]
	v_add_co_u32_e64 v120, s[0:1], s33, v32
	v_mov_b32_e32 v8, 0
	s_nop 0
	v_addc_co_u32_e64 v121, s[0:1], 0, v33, s[0:1]
	v_add_co_u32_e64 v124, s[0:1], s34, v32
	v_mov_b32_e32 v9, 0
	s_nop 0
	v_addc_co_u32_e64 v125, s[0:1], 0, v33, s[0:1]
	v_add_co_u32_e64 v128, s[0:1], s35, v32
	v_mov_b32_e32 v10, 0
	s_nop 0
	v_addc_co_u32_e64 v129, s[0:1], 0, v33, s[0:1]
	v_add_co_u32_e64 v132, s[0:1], s60, v32
	v_mov_b32_e32 v11, 0
	s_nop 0
	v_addc_co_u32_e64 v133, s[0:1], 0, v33, s[0:1]
	v_add_co_u32_e64 v136, s[0:1], s61, v32
	v_mov_b32_e32 v12, 0
	s_nop 0
	v_addc_co_u32_e64 v137, s[0:1], 0, v33, s[0:1]
	v_add_co_u32_e64 v140, s[0:1], s62, v32
	v_mov_b32_e32 v13, 0
	s_nop 0
	v_addc_co_u32_e64 v141, s[0:1], 0, v33, s[0:1]
	v_add_co_u32_e64 v144, s[0:1], s63, v32
	v_mov_b32_e32 v14, 0
	s_nop 0
	v_addc_co_u32_e64 v145, s[0:1], 0, v33, s[0:1]
	v_add_co_u32_e64 v32, s[0:1], s64, v32
	v_mov_b32_e32 v15, 0
	s_nop 0
	v_addc_co_u32_e64 v33, s[0:1], 0, v33, s[0:1]
	global_load_dwordx4 v[92:95], v[34:35], off nt
	global_load_dwordx4 v[96:99], v[36:37], off nt
	s_nop 0
	global_load_dwordx4 v[100:103], v[100:101], off nt
	s_nop 0
	global_load_dwordx4 v[104:107], v[104:105], off nt
	s_nop 0
	global_load_dwordx4 v[108:111], v[108:109], off nt
	s_nop 0
	global_load_dwordx4 v[112:115], v[112:113], off nt
	s_nop 0
	global_load_dwordx4 v[116:119], v[116:117], off nt
	s_nop 0
	global_load_dwordx4 v[120:123], v[120:121], off nt
	s_nop 0
	global_load_dwordx4 v[124:127], v[124:125], off nt
	s_nop 0
	global_load_dwordx4 v[128:131], v[128:129], off nt
	s_nop 0
	global_load_dwordx4 v[132:135], v[132:133], off nt
	s_nop 0
	global_load_dwordx4 v[136:139], v[136:137], off nt
	s_nop 0
	global_load_dwordx4 v[140:143], v[140:141], off nt
	s_nop 0
	global_load_dwordx4 v[144:147], v[144:145], off nt
	s_nop 0
	global_load_dwordx4 v[148:151], v[32:33], off nt
	v_mov_b32_e32 v16, 0
	v_mov_b32_e32 v17, 0
	v_or_b32_e32 v152, v154, v66
	v_sub_u32_e32 v38, v86, v38
	v_lshlrev_b64 v[32:33], 11, v[152:153]
	v_or_b32_e32 v152, v154, v68
	v_ashrrev_i32_e32 v39, 31, v38
	v_lshlrev_b64 v[34:35], 11, v[152:153]
	v_or_b32_e32 v152, v154, v70
	v_lshl_add_u64 v[38:39], v[18:19], 0, v[38:39]
	v_lshlrev_b64 v[36:37], 11, v[152:153]
	v_or_b32_e32 v152, v154, v72
	v_lshl_add_u64 v[32:33], v[38:39], 0, v[32:33]
	v_lshlrev_b64 v[152:153], 11, v[152:153]
	v_lshl_add_u64 v[34:35], v[38:39], 0, v[34:35]
	v_lshl_add_u64 v[36:37], v[38:39], 0, v[36:37]
	v_lshl_add_u64 v[38:39], v[38:39], 0, v[152:153]
	v_add_u32_e32 v87, s3, v87
	v_cmp_lt_i32_e64 s[6:7], s66, v87
	v_add_u32_e32 v30, s23, v30
	s_or_b64 s[16:17], s[6:7], s[16:17]
	v_add_u32_e32 v86, s67, v86
	s_waitcnt vmcnt(15)
	ds_write2_b32 v40, v88, v89 offset1:1
	ds_write2_b32 v40, v90, v91 offset0:2 offset1:3
	s_waitcnt vmcnt(14)
	ds_write2_b32 v41, v92, v93 offset1:1
	ds_write2_b32 v42, v94, v95 offset1:1
	s_waitcnt vmcnt(13)
	ds_write2_b32 v43, v96, v97 offset1:1
	ds_write2_b32 v44, v98, v99 offset1:1
	s_waitcnt vmcnt(12)
	ds_write2_b32 v45, v100, v101 offset1:1
	ds_write2_b32 v46, v102, v103 offset1:1
	s_waitcnt vmcnt(11)
	ds_write2_b32 v47, v104, v105 offset1:1
	ds_write2_b32 v48, v106, v107 offset1:1
	s_waitcnt vmcnt(10)
	ds_write2_b32 v49, v108, v109 offset1:1
	ds_write2_b32 v50, v110, v111 offset1:1
	s_waitcnt vmcnt(9)
	ds_write2_b32 v51, v112, v113 offset1:1
	ds_write2_b32 v52, v114, v115 offset1:1
	s_waitcnt vmcnt(8)
	ds_write2_b32 v53, v116, v117 offset1:1
	ds_write2_b32 v54, v118, v119 offset1:1
	s_waitcnt vmcnt(7)
	ds_write2_b32 v55, v120, v121 offset1:1
	ds_write2_b32 v56, v122, v123 offset1:1
	s_waitcnt vmcnt(6)
	ds_write2_b32 v57, v124, v125 offset1:1
	ds_write2_b32 v58, v126, v127 offset1:1
	s_waitcnt vmcnt(5)
	ds_write2_b32 v59, v128, v129 offset1:1
	ds_write2_b32 v60, v130, v131 offset1:1
	s_waitcnt vmcnt(4)
	ds_write2_b32 v61, v132, v133 offset1:1
	ds_write2_b32 v62, v134, v135 offset1:1
	s_waitcnt vmcnt(3)
	ds_write2_b32 v63, v136, v137 offset1:1
	ds_write2_b32 v64, v138, v139 offset1:1
	s_waitcnt vmcnt(2)
	ds_write2_b32 v71, v140, v141 offset1:1
	ds_write2_b32 v73, v142, v143 offset1:1
	s_waitcnt vmcnt(1)
	ds_write2_b32 v76, v144, v145 offset1:1
	ds_write2_b32 v77, v146, v147 offset1:1
	s_waitcnt vmcnt(0)
	ds_write2_b32 v82, v148, v149 offset1:1
	ds_write2_b32 v83, v150, v151 offset1:1
	s_waitcnt lgkmcnt(0)
	ds_read2_b32 v[88:89], v75 offset1:8
	ds_read2_b32 v[90:91], v75 offset0:33 offset1:41
	ds_read2_b32 v[92:93], v75 offset0:66 offset1:74
	ds_read2_b32 v[94:95], v75 offset0:99 offset1:107
	ds_read2_b32 v[96:97], v75 offset0:132 offset1:140
	ds_read2_b32 v[98:99], v75 offset0:165 offset1:173
	ds_read2_b32 v[100:101], v84 offset0:8 offset1:16
	ds_read2_b32 v[102:103], v84 offset0:41 offset1:49
	ds_read2_b32 v[104:105], v84 offset0:140 offset1:148
	ds_read2_b32 v[106:107], v84 offset0:173 offset1:181
	ds_read2_b32 v[108:109], v75 offset0:16 offset1:24
	ds_read2_b32 v[110:111], v75 offset0:49 offset1:57
	ds_read2_b32 v[112:113], v75 offset0:148 offset1:156
	ds_read2_b32 v[114:115], v75 offset0:181 offset1:189
	ds_read2_b32 v[116:117], v84 offset0:24 offset1:32
	ds_read2_b32 v[118:119], v84 offset0:57 offset1:65
	ds_read2_b32 v[120:121], v84 offset0:156 offset1:164
	ds_read2_b32 v[122:123], v84 offset0:189 offset1:197
	ds_read2_b32 v[124:125], v75 offset0:198 offset1:206
	ds_read2_b32 v[126:127], v75 offset0:231 offset1:239
	ds_read2_b32 v[128:129], v84 offset0:74 offset1:82
	ds_read2_b32 v[130:131], v84 offset0:107 offset1:115
	ds_read2_b32 v[132:133], v84 offset0:206 offset1:214
	ds_read2_b32 v[134:135], v84 offset0:239 offset1:247
	ds_read2_b32 v[136:137], v75 offset0:82 offset1:90
	ds_read2_b32 v[138:139], v75 offset0:115 offset1:123
	ds_read2_b32 v[140:141], v75 offset0:214 offset1:222
	ds_read2_b32 v[142:143], v75 offset0:247 offset1:255
	ds_read2_b32 v[144:145], v84 offset0:90 offset1:98
	ds_read2_b32 v[146:147], v84 offset0:123 offset1:131
	ds_read2_b32 v[148:149], v84 offset0:222 offset1:230
	ds_read2_b32 v[150:151], v85 offset0:127 offset1:135
	s_waitcnt lgkmcnt(14)
	v_mul_f32_e32 v88, 0x43800000, v88
	v_mul_f32_e32 v90, 0x43800000, v90
	v_mul_f32_e32 v96, 0x43800000, v96
	v_mul_f32_e32 v98, 0x43800000, v98
	v_mul_f32_e32 v100, 0x43800000, v100
	v_mul_f32_e32 v102, 0x43800000, v102
	v_mul_f32_e32 v104, 0x43800000, v104
	v_mul_f32_e32 v106, 0x43800000, v106
	v_mul_f32_e32 v89, 0x43800000, v89
	v_mul_f32_e32 v91, 0x43800000, v91
	v_mul_f32_e32 v97, 0x43800000, v97
	v_mul_f32_e32 v99, 0x43800000, v99
	v_mul_f32_e32 v101, 0x43800000, v101
	v_mul_f32_e32 v103, 0x43800000, v103
	v_mul_f32_e32 v105, 0x43800000, v105
	v_mul_f32_e32 v107, 0x43800000, v107
	v_med3_f32 v88, v88, s65, v65
	v_med3_f32 v90, v90, s65, v65
	v_med3_f32 v96, v96, s65, v65
	v_med3_f32 v98, v98, s65, v65
	v_med3_f32 v100, v100, s65, v65
	v_med3_f32 v102, v102, s65, v65
	v_med3_f32 v104, v104, s65, v65
	v_med3_f32 v106, v106, s65, v65
	v_mul_f32_e32 v108, 0x43800000, v108
	v_mul_f32_e32 v110, 0x43800000, v110
	v_mul_f32_e32 v112, 0x43800000, v112
	v_mul_f32_e32 v114, 0x43800000, v114
	v_mul_f32_e32 v116, 0x43800000, v116
	v_mul_f32_e32 v118, 0x43800000, v118
	v_mul_f32_e32 v120, 0x43800000, v120
	v_mul_f32_e32 v122, 0x43800000, v122
	v_med3_f32 v89, v89, s65, v65
	v_med3_f32 v91, v91, s65, v65
	v_med3_f32 v97, v97, s65, v65
	v_med3_f32 v99, v99, s65, v65
	v_med3_f32 v101, v101, s65, v65
	v_med3_f32 v103, v103, s65, v65
	v_med3_f32 v105, v105, s65, v65
	v_med3_f32 v107, v107, s65, v65
	v_cvt_pk_fp8_f32 v2, v88, v90
	v_cvt_pk_fp8_f32 v3, v96, v98
	v_cvt_pk_fp8_f32 v4, v100, v102
	v_cvt_pk_fp8_f32 v5, v104, v106
	v_mul_f32_e32 v109, 0x43800000, v109
	v_mul_f32_e32 v111, 0x43800000, v111
	v_mul_f32_e32 v113, 0x43800000, v113
	v_mul_f32_e32 v115, 0x43800000, v115
	v_mul_f32_e32 v117, 0x43800000, v117
	v_mul_f32_e32 v119, 0x43800000, v119
	v_mul_f32_e32 v121, 0x43800000, v121
	v_mul_f32_e32 v123, 0x43800000, v123
	v_med3_f32 v108, v108, s65, v65
	v_med3_f32 v110, v110, s65, v65
	v_med3_f32 v112, v112, s65, v65
	v_med3_f32 v114, v114, s65, v65
	v_med3_f32 v116, v116, s65, v65
	v_med3_f32 v118, v118, s65, v65
	v_med3_f32 v120, v120, s65, v65
	v_med3_f32 v122, v122, s65, v65
	v_cvt_pk_fp8_f32 v6, v89, v91
	v_cvt_pk_fp8_f32 v7, v97, v99
	v_cvt_pk_fp8_f32 v8, v101, v103
	v_cvt_pk_fp8_f32 v9, v105, v107
	v_mul_f32_e32 v92, 0x43800000, v92
	v_mul_f32_e32 v94, 0x43800000, v94
	s_waitcnt lgkmcnt(13)
	v_mul_f32_e32 v124, 0x43800000, v124
	s_waitcnt lgkmcnt(12)
	v_mul_f32_e32 v126, 0x43800000, v126
	s_waitcnt lgkmcnt(11)
	v_mul_f32_e32 v128, 0x43800000, v128
	s_waitcnt lgkmcnt(10)
	v_mul_f32_e32 v130, 0x43800000, v130
	s_waitcnt lgkmcnt(9)
	v_mul_f32_e32 v132, 0x43800000, v132
	s_waitcnt lgkmcnt(8)
	v_mul_f32_e32 v134, 0x43800000, v134
	v_med3_f32 v109, v109, s65, v65
	v_med3_f32 v111, v111, s65, v65
	v_med3_f32 v113, v113, s65, v65
	v_med3_f32 v115, v115, s65, v65
	v_med3_f32 v117, v117, s65, v65
	v_med3_f32 v119, v119, s65, v65
	v_med3_f32 v121, v121, s65, v65
	v_med3_f32 v123, v123, s65, v65
	v_cvt_pk_fp8_f32 v10, v108, v110
	v_cvt_pk_fp8_f32 v11, v112, v114
	v_cvt_pk_fp8_f32 v12, v116, v118
	v_cvt_pk_fp8_f32 v13, v120, v122
	v_mul_f32_e32 v93, 0x43800000, v93
	v_mul_f32_e32 v95, 0x43800000, v95
	v_mul_f32_e32 v125, 0x43800000, v125
	v_mul_f32_e32 v127, 0x43800000, v127
	v_mul_f32_e32 v129, 0x43800000, v129
	v_mul_f32_e32 v131, 0x43800000, v131
	v_mul_f32_e32 v133, 0x43800000, v133
	v_mul_f32_e32 v135, 0x43800000, v135
	v_med3_f32 v92, v92, s65, v65
	v_med3_f32 v94, v94, s65, v65
	v_med3_f32 v124, v124, s65, v65
	v_med3_f32 v126, v126, s65, v65
	v_med3_f32 v128, v128, s65, v65
	v_med3_f32 v130, v130, s65, v65
	v_med3_f32 v132, v132, s65, v65
	v_med3_f32 v134, v134, s65, v65
	v_cvt_pk_fp8_f32 v14, v109, v111
	v_cvt_pk_fp8_f32 v15, v113, v115
	v_cvt_pk_fp8_f32 v16, v117, v119
	v_cvt_pk_fp8_f32 v17, v121, v123
	s_waitcnt lgkmcnt(7)
	v_mul_f32_e32 v136, 0x43800000, v136
	s_waitcnt lgkmcnt(6)
	v_mul_f32_e32 v138, 0x43800000, v138
	s_waitcnt lgkmcnt(5)
	v_mul_f32_e32 v140, 0x43800000, v140
	s_waitcnt lgkmcnt(4)
	v_mul_f32_e32 v142, 0x43800000, v142
	s_waitcnt lgkmcnt(3)
	v_mul_f32_e32 v144, 0x43800000, v144
	s_waitcnt lgkmcnt(2)
	v_mul_f32_e32 v146, 0x43800000, v146
	s_waitcnt lgkmcnt(1)
	v_mul_f32_e32 v148, 0x43800000, v148
	s_waitcnt lgkmcnt(0)
	v_mul_f32_e32 v150, 0x43800000, v150
	v_med3_f32 v93, v93, s65, v65
	v_med3_f32 v95, v95, s65, v65
	v_med3_f32 v125, v125, s65, v65
	v_med3_f32 v127, v127, s65, v65
	v_med3_f32 v129, v129, s65, v65
	v_med3_f32 v131, v131, s65, v65
	v_med3_f32 v133, v133, s65, v65
	v_med3_f32 v135, v135, s65, v65
	v_cvt_pk_fp8_f32 v2, v92, v94 op_sel:[0,0,1]
	v_cvt_pk_fp8_f32 v3, v124, v126 op_sel:[0,0,1]
	v_cvt_pk_fp8_f32 v4, v128, v130 op_sel:[0,0,1]
	v_cvt_pk_fp8_f32 v5, v132, v134 op_sel:[0,0,1]
	v_mul_f32_e32 v137, 0x43800000, v137
	v_mul_f32_e32 v139, 0x43800000, v139
	v_mul_f32_e32 v141, 0x43800000, v141
	v_mul_f32_e32 v143, 0x43800000, v143
	v_mul_f32_e32 v145, 0x43800000, v145
	v_mul_f32_e32 v147, 0x43800000, v147
	v_mul_f32_e32 v149, 0x43800000, v149
	v_mul_f32_e32 v151, 0x43800000, v151
	v_med3_f32 v136, v136, s65, v65
	v_med3_f32 v138, v138, s65, v65
	v_med3_f32 v140, v140, s65, v65
	v_med3_f32 v142, v142, s65, v65
	v_med3_f32 v144, v144, s65, v65
	v_med3_f32 v146, v146, s65, v65
	v_med3_f32 v148, v148, s65, v65
	v_med3_f32 v150, v150, s65, v65
	v_cvt_pk_fp8_f32 v6, v93, v95 op_sel:[0,0,1]
	v_cvt_pk_fp8_f32 v7, v125, v127 op_sel:[0,0,1]
	v_cvt_pk_fp8_f32 v8, v129, v131 op_sel:[0,0,1]
	v_cvt_pk_fp8_f32 v9, v133, v135 op_sel:[0,0,1]
	v_med3_f32 v137, v137, s65, v65
	v_med3_f32 v139, v139, s65, v65
	v_med3_f32 v141, v141, s65, v65
	v_med3_f32 v143, v143, s65, v65
	v_med3_f32 v145, v145, s65, v65
	v_med3_f32 v147, v147, s65, v65
	v_med3_f32 v149, v149, s65, v65
	v_med3_f32 v151, v151, s65, v65
	v_cvt_pk_fp8_f32 v10, v136, v138 op_sel:[0,0,1]
	v_cvt_pk_fp8_f32 v11, v140, v142 op_sel:[0,0,1]
	v_cvt_pk_fp8_f32 v12, v144, v146 op_sel:[0,0,1]
	v_cvt_pk_fp8_f32 v13, v148, v150 op_sel:[0,0,1]
	v_cvt_pk_fp8_f32 v14, v137, v139 op_sel:[0,0,1]
	v_cvt_pk_fp8_f32 v15, v141, v143 op_sel:[0,0,1]
	v_cvt_pk_fp8_f32 v16, v145, v147 op_sel:[0,0,1]
	v_cvt_pk_fp8_f32 v17, v149, v151 op_sel:[0,0,1]
	global_store_dwordx4 v[32:33], v[2:5], off nt
	global_store_dwordx4 v[34:35], v[6:9], off nt
	global_store_dwordx4 v[36:37], v[10:13], off nt
	global_store_dwordx4 v[38:39], v[14:17], off nt
	s_waitcnt lgkmcnt(0)
	s_andn2_b64 exec, exec, s[16:17]
	s_cbranch_execnz .LBB0_12
	s_or_b64 exec, exec, s[16:17]
	s_mov_b64 exec, -1
	s_lshl_b64 s[6:7], s[8:9], 11
	v_mad_u64_u32 v[28:29], s[0:1], s8, v67, v[26:27]
	s_mov_b64 s[14:15], 0
	v_mov_b32_e32 v30, v74
	v_mov_b32_e32 v86, v69
	s_cmp_eq_u32 s99, 2
	s_cbranch_scc0 .Lnsk14
	s_mov_b64 exec, 0
.Lnsk14:
.LBB0_14:
	s_mov_b32 s0, 0x92492493
	v_mul_hi_i32 v32, v86, s0
	v_add_u32_e32 v32, v32, v86
	v_lshrrev_b32_e32 v33, 31, v32
	v_ashrrev_i32_e32 v32, 5, v32
	v_add_u32_e32 v33, v32, v33
	s_movk_i32 s0, 0xe400
	v_lshlrev_b32_e32 v32, 5, v33
	v_mad_u64_u32 v[34:35], s[0:1], v33, s0, v[30:31]
	v_ashrrev_i32_e32 v33, 31, v32
	v_add_u32_e32 v36, v34, v66
	v_ashrrev_i32_e32 v35, 31, v34
	v_lshl_add_u64 v[92:93], s[6:7], 0, v[32:33]
	v_lshl_add_u64 v[94:95], v[32:33], 2, v[28:29]
	v_ashrrev_i32_e32 v37, 31, v36
	v_add_u32_e32 v32, 8, v36
	v_add_u32_e32 v38, 16, v36
	v_add_u32_e32 v88, 24, v36
	v_add_u32_e32 v90, 32, v36
	v_add_u32_e32 v96, 40, v36
	v_add_u32_e32 v98, 48, v36
	v_add_u32_e32 v100, 56, v36
	v_add_u32_e32 v102, 64, v36
	v_add_u32_e32 v104, 0x48, v36
	v_add_u32_e32 v106, 0x50, v36
	v_add_u32_e32 v108, 0x58, v36
	v_add_u32_e32 v110, 0x60, v36
	v_add_u32_e32 v112, 0x68, v36
	v_add_u32_e32 v114, 0x70, v36
	v_add_u32_e32 v116, 0x78, v36
	v_lshl_add_u64 v[118:119], v[20:21], 0, v[34:35]
	v_lshlrev_b64 v[34:35], 13, v[36:37]
	v_ashrrev_i32_e32 v33, 31, v32
	v_ashrrev_i32_e32 v39, 31, v38
	v_ashrrev_i32_e32 v89, 31, v88
	v_ashrrev_i32_e32 v91, 31, v90
	v_ashrrev_i32_e32 v97, 31, v96
	v_ashrrev_i32_e32 v99, 31, v98
	v_ashrrev_i32_e32 v101, 31, v100
	v_ashrrev_i32_e32 v103, 31, v102
	v_ashrrev_i32_e32 v105, 31, v104
	v_ashrrev_i32_e32 v107, 31, v106
	v_ashrrev_i32_e32 v109, 31, v108
	v_ashrrev_i32_e32 v111, 31, v110
	v_ashrrev_i32_e32 v113, 31, v112
	v_ashrrev_i32_e32 v115, 31, v114
	v_ashrrev_i32_e32 v117, 31, v116
	v_or_b32_e32 v36, v92, v66
	v_or_b32_e32 v37, v92, v68
	v_or_b32_e32 v87, v92, v70
	v_or_b32_e32 v92, v92, v72
	v_lshl_add_u64 v[120:121], v[94:95], 0, v[34:35]
	v_lshlrev_b64 v[122:123], 13, v[32:33]
	v_lshlrev_b64 v[124:125], 13, v[38:39]
	v_lshlrev_b64 v[126:127], 13, v[88:89]
	v_lshlrev_b64 v[128:129], 13, v[90:91]
	v_lshlrev_b64 v[96:97], 13, v[96:97]
	v_lshlrev_b64 v[98:99], 13, v[98:99]
	v_lshlrev_b64 v[100:101], 13, v[100:101]
	v_lshlrev_b64 v[102:103], 13, v[102:103]
	v_lshlrev_b64 v[104:105], 13, v[104:105]
	v_lshlrev_b64 v[106:107], 13, v[106:107]
	v_lshlrev_b64 v[108:109], 13, v[108:109]
	v_lshlrev_b64 v[110:111], 13, v[110:111]
	v_lshlrev_b64 v[112:113], 13, v[112:113]
	v_lshlrev_b64 v[114:115], 13, v[114:115]
	v_lshlrev_b64 v[116:117], 13, v[116:117]
	v_mad_u64_u32 v[38:39], s[0:1], v36, s21, v[118:119]
	v_mad_u64_u32 v[36:37], s[0:1], v37, s21, v[118:119]
	v_mad_u64_u32 v[34:35], s[0:1], v87, s21, v[118:119]
	v_mad_u64_u32 v[32:33], s[0:1], v92, s21, v[118:119]
	global_load_dwordx4 v[88:91], v[120:121], off nt
	v_lshl_add_u64 v[118:119], v[94:95], 0, v[122:123]
	v_lshl_add_u64 v[120:121], v[94:95], 0, v[124:125]
	v_lshl_add_u64 v[122:123], v[94:95], 0, v[126:127]
	v_lshl_add_u64 v[124:125], v[94:95], 0, v[128:129]
	v_lshl_add_u64 v[126:127], v[94:95], 0, v[96:97]
	v_lshl_add_u64 v[128:129], v[94:95], 0, v[98:99]
	v_lshl_add_u64 v[130:131], v[94:95], 0, v[100:101]
	v_lshl_add_u64 v[132:133], v[94:95], 0, v[102:103]
	v_lshl_add_u64 v[134:135], v[94:95], 0, v[104:105]
	v_lshl_add_u64 v[136:137], v[94:95], 0, v[106:107]
	v_lshl_add_u64 v[138:139], v[94:95], 0, v[108:109]
	v_lshl_add_u64 v[140:141], v[94:95], 0, v[110:111]
	v_lshl_add_u64 v[142:143], v[94:95], 0, v[112:113]
	v_lshl_add_u64 v[144:145], v[94:95], 0, v[114:115]
	v_lshl_add_u64 v[148:149], v[94:95], 0, v[116:117]
	v_mad_i32_i24 v39, v93, s21, v39
	v_mad_i32_i24 v37, v93, s21, v37
	v_mad_i32_i24 v35, v93, s21, v35
	v_mad_i32_i24 v33, v93, s21, v33
	global_load_dwordx4 v[92:95], v[118:119], off nt
	global_load_dwordx4 v[96:99], v[120:121], off nt
	global_load_dwordx4 v[100:103], v[122:123], off nt
	global_load_dwordx4 v[104:107], v[124:125], off nt
	global_load_dwordx4 v[108:111], v[126:127], off nt
	global_load_dwordx4 v[112:115], v[128:129], off nt
	global_load_dwordx4 v[116:119], v[130:131], off nt
	s_nop 0
	global_load_dwordx4 v[120:123], v[132:133], off nt
	global_load_dwordx4 v[124:127], v[134:135], off nt
	global_load_dwordx4 v[128:131], v[136:137], off nt
	s_nop 0
	global_load_dwordx4 v[132:135], v[138:139], off nt
	s_nop 0
	global_load_dwordx4 v[136:139], v[140:141], off nt
	s_nop 0
	global_load_dwordx4 v[140:143], v[142:143], off nt
	s_nop 0
	global_load_dwordx4 v[144:147], v[144:145], off nt
	s_nop 0
	global_load_dwordx4 v[148:151], v[148:149], off nt
	s_waitcnt vmcnt(15)
	ds_write2_b32 v40, v88, v89 offset1:1
	ds_write2_b32 v40, v90, v91 offset0:2 offset1:3
	s_waitcnt vmcnt(14)
	ds_write2_b32 v41, v92, v93 offset1:1
	ds_write2_b32 v42, v94, v95 offset1:1
	s_waitcnt vmcnt(13)
	ds_write2_b32 v43, v96, v97 offset1:1
	ds_write2_b32 v44, v98, v99 offset1:1
	s_waitcnt vmcnt(12)
	ds_write2_b32 v45, v100, v101 offset1:1
	ds_write2_b32 v46, v102, v103 offset1:1
	s_waitcnt vmcnt(11)
	ds_write2_b32 v47, v104, v105 offset1:1
	ds_write2_b32 v48, v106, v107 offset1:1
	s_waitcnt vmcnt(10)
	ds_write2_b32 v49, v108, v109 offset1:1
	ds_write2_b32 v50, v110, v111 offset1:1
	s_waitcnt vmcnt(9)
	ds_write2_b32 v51, v112, v113 offset1:1
	ds_write2_b32 v52, v114, v115 offset1:1
	s_waitcnt vmcnt(8)
	ds_write2_b32 v53, v116, v117 offset1:1
	ds_write2_b32 v54, v118, v119 offset1:1
	s_waitcnt vmcnt(7)
	ds_write2_b32 v55, v120, v121 offset1:1
	ds_write2_b32 v56, v122, v123 offset1:1
	s_waitcnt vmcnt(6)
	ds_write2_b32 v57, v124, v125 offset1:1
	ds_write2_b32 v58, v126, v127 offset1:1
	s_waitcnt vmcnt(5)
	ds_write2_b32 v59, v128, v129 offset1:1
	ds_write2_b32 v60, v130, v131 offset1:1
	s_waitcnt vmcnt(4)
	ds_write2_b32 v61, v132, v133 offset1:1
	ds_write2_b32 v62, v134, v135 offset1:1
	s_waitcnt vmcnt(3)
	ds_write2_b32 v63, v136, v137 offset1:1
	ds_write2_b32 v64, v138, v139 offset1:1
	s_waitcnt vmcnt(2)
	ds_write2_b32 v71, v140, v141 offset1:1
	ds_write2_b32 v73, v142, v143 offset1:1
	s_waitcnt vmcnt(1)
	ds_write2_b32 v76, v144, v145 offset1:1
	ds_write2_b32 v77, v146, v147 offset1:1
	s_waitcnt vmcnt(0)
	ds_write2_b32 v82, v148, v149 offset1:1
	ds_write2_b32 v83, v150, v151 offset1:1
	s_waitcnt lgkmcnt(0)
	ds_read2_b32 v[88:89], v75 offset1:8
	ds_read2_b32 v[90:91], v75 offset0:33 offset1:41
	ds_read2_b32 v[92:93], v75 offset0:66 offset1:74
	ds_read2_b32 v[94:95], v75 offset0:99 offset1:107
	ds_read2_b32 v[96:97], v75 offset0:132 offset1:140
	ds_read2_b32 v[98:99], v75 offset0:165 offset1:173
	ds_read2_b32 v[100:101], v75 offset0:198 offset1:206
	ds_read2_b32 v[102:103], v75 offset0:231 offset1:239
	ds_read2_b32 v[104:105], v84 offset0:8 offset1:16
	ds_read2_b32 v[106:107], v84 offset0:41 offset1:49
	ds_read2_b32 v[108:109], v84 offset0:74 offset1:82
	ds_read2_b32 v[110:111], v84 offset0:107 offset1:115
	ds_read2_b32 v[112:113], v84 offset0:140 offset1:148
	ds_read2_b32 v[114:115], v84 offset0:173 offset1:181
	ds_read2_b32 v[116:117], v84 offset0:206 offset1:214
	ds_read2_b32 v[118:119], v84 offset0:239 offset1:247
	ds_read2_b32 v[120:121], v75 offset0:16 offset1:24
	ds_read2_b32 v[122:123], v75 offset0:49 offset1:57
	ds_read2_b32 v[124:125], v75 offset0:82 offset1:90
	ds_read2_b32 v[126:127], v75 offset0:115 offset1:123
	ds_read2_b32 v[128:129], v75 offset0:148 offset1:156
	ds_read2_b32 v[130:131], v75 offset0:181 offset1:189
	ds_read2_b32 v[132:133], v75 offset0:214 offset1:222
	ds_read2_b32 v[134:135], v75 offset0:247 offset1:255
	ds_read2_b32 v[136:137], v84 offset0:24 offset1:32
	ds_read2_b32 v[138:139], v84 offset0:57 offset1:65
	ds_read2_b32 v[140:141], v84 offset0:90 offset1:98
	ds_read2_b32 v[142:143], v84 offset0:123 offset1:131
	ds_read2_b32 v[144:145], v84 offset0:156 offset1:164
	ds_read2_b32 v[146:147], v84 offset0:189 offset1:197
	ds_read2_b32 v[148:149], v84 offset0:222 offset1:230
	ds_read2_b32 v[150:151], v85 offset0:127 offset1:135
	s_waitcnt lgkmcnt(14)
	v_mul_f32_e32 v87, 0x43800000, v88
	v_mul_f32_e32 v88, 0x43800000, v90
	v_mul_f32_e32 v90, 0x43800000, v92
	v_mul_f32_e32 v92, 0x43800000, v94
	v_mul_f32_e32 v94, 0x43800000, v96
	v_mul_f32_e32 v96, 0x43800000, v98
	v_mul_f32_e32 v98, 0x43800000, v100
	v_mul_f32_e32 v100, 0x43800000, v102
	v_mul_f32_e32 v102, 0x43800000, v104
	v_mul_f32_e32 v104, 0x43800000, v106
	v_mul_f32_e32 v106, 0x43800000, v108
	v_mul_f32_e32 v108, 0x43800000, v110
	v_mul_f32_e32 v110, 0x43800000, v112
	v_mul_f32_e32 v112, 0x43800000, v114
	v_mov_b32_e32 v2, 0
	v_mov_b32_e32 v3, 0
	v_mov_b32_e32 v4, 0
	v_mov_b32_e32 v5, 0
	v_mul_f32_e32 v89, 0x43800000, v89
	v_mul_f32_e32 v91, 0x43800000, v91
	v_mul_f32_e32 v97, 0x43800000, v97
	v_mul_f32_e32 v99, 0x43800000, v99
	v_mul_f32_e32 v105, 0x43800000, v105
	v_mul_f32_e32 v107, 0x43800000, v107
	v_mul_f32_e32 v113, 0x43800000, v113
	v_mul_f32_e32 v115, 0x43800000, v115
	v_med3_f32 v87, v87, s65, v65
	v_med3_f32 v88, v88, s65, v65
	v_med3_f32 v94, v94, s65, v65
	v_med3_f32 v96, v96, s65, v65
	v_med3_f32 v102, v102, s65, v65
	v_med3_f32 v104, v104, s65, v65
	v_med3_f32 v110, v110, s65, v65
	v_med3_f32 v112, v112, s65, v65
	v_mov_b32_e32 v6, 0
	v_mov_b32_e32 v7, 0
	v_mov_b32_e32 v8, 0
	v_mov_b32_e32 v9, 0
	v_mul_f32_e32 v114, 0x43800000, v116
	v_mul_f32_e32 v116, 0x43800000, v118
	v_mul_f32_e32 v118, 0x43800000, v119
	v_mul_f32_e32 v119, 0x43800000, v120
	v_mul_f32_e32 v120, 0x43800000, v122
	s_waitcnt lgkmcnt(13)
	v_mul_f32_e32 v122, 0x43800000, v124
	s_waitcnt lgkmcnt(12)
	v_mul_f32_e32 v124, 0x43800000, v126
	s_waitcnt lgkmcnt(11)
	v_mul_f32_e32 v126, 0x43800000, v128
	s_waitcnt lgkmcnt(10)
	v_mul_f32_e32 v128, 0x43800000, v130
	s_waitcnt lgkmcnt(9)
	v_mul_f32_e32 v130, 0x43800000, v132
	s_waitcnt lgkmcnt(8)
	v_mul_f32_e32 v132, 0x43800000, v134
	s_waitcnt lgkmcnt(7)
	v_mul_f32_e32 v134, 0x43800000, v136
	s_waitcnt lgkmcnt(6)
	v_mul_f32_e32 v136, 0x43800000, v138
	s_waitcnt lgkmcnt(5)
	v_mul_f32_e32 v138, 0x43800000, v140
	s_waitcnt lgkmcnt(4)
	v_mul_f32_e32 v140, 0x43800000, v142
	s_waitcnt lgkmcnt(3)
	v_mul_f32_e32 v142, 0x43800000, v144
	s_waitcnt lgkmcnt(2)
	v_mul_f32_e32 v144, 0x43800000, v146
	v_med3_f32 v89, v89, s65, v65
	v_med3_f32 v91, v91, s65, v65
	v_med3_f32 v97, v97, s65, v65
	v_med3_f32 v99, v99, s65, v65
	v_med3_f32 v105, v105, s65, v65
	v_med3_f32 v107, v107, s65, v65
	v_med3_f32 v113, v113, s65, v65
	v_med3_f32 v115, v115, s65, v65
	v_cvt_pk_fp8_f32 v2, v87, v88
	v_cvt_pk_fp8_f32 v3, v94, v96
	v_cvt_pk_fp8_f32 v4, v102, v104
	v_cvt_pk_fp8_f32 v5, v110, v112
	v_mov_b32_e32 v10, 0
	v_mov_b32_e32 v11, 0
	v_mov_b32_e32 v12, 0
	v_mov_b32_e32 v13, 0
	v_mul_f32_e32 v121, 0x43800000, v121
	v_mul_f32_e32 v123, 0x43800000, v123
	v_mul_f32_e32 v129, 0x43800000, v129
	v_mul_f32_e32 v131, 0x43800000, v131
	v_mul_f32_e32 v137, 0x43800000, v137
	v_mul_f32_e32 v139, 0x43800000, v139
	v_mul_f32_e32 v145, 0x43800000, v145
	v_mul_f32_e32 v147, 0x43800000, v147
	v_med3_f32 v119, v119, s65, v65
	v_med3_f32 v120, v120, s65, v65
	v_med3_f32 v126, v126, s65, v65
	v_med3_f32 v128, v128, s65, v65
	v_med3_f32 v134, v134, s65, v65
	v_med3_f32 v136, v136, s65, v65
	v_med3_f32 v142, v142, s65, v65
	v_med3_f32 v144, v144, s65, v65
	v_cvt_pk_fp8_f32 v6, v89, v91
	v_cvt_pk_fp8_f32 v7, v97, v99
	v_cvt_pk_fp8_f32 v8, v105, v107
	v_cvt_pk_fp8_f32 v9, v113, v115
	v_mov_b32_e32 v14, 0
	v_mov_b32_e32 v15, 0
	v_mov_b32_e32 v16, 0
	v_mov_b32_e32 v17, 0
	v_med3_f32 v121, v121, s65, v65
	v_med3_f32 v123, v123, s65, v65
	v_med3_f32 v129, v129, s65, v65
	v_med3_f32 v131, v131, s65, v65
	v_med3_f32 v137, v137, s65, v65
	v_med3_f32 v139, v139, s65, v65
	v_med3_f32 v145, v145, s65, v65
	v_med3_f32 v147, v147, s65, v65
	v_cvt_pk_fp8_f32 v10, v119, v120
	v_cvt_pk_fp8_f32 v11, v126, v128
	v_cvt_pk_fp8_f32 v12, v134, v136
	v_cvt_pk_fp8_f32 v13, v142, v144
	v_mul_f32_e32 v93, 0x43800000, v93
	v_mul_f32_e32 v95, 0x43800000, v95
	v_mul_f32_e32 v101, 0x43800000, v101
	v_mul_f32_e32 v103, 0x43800000, v103
	v_mul_f32_e32 v109, 0x43800000, v109
	v_mul_f32_e32 v111, 0x43800000, v111
	v_mul_f32_e32 v117, 0x43800000, v117
	v_med3_f32 v90, v90, s65, v65
	v_med3_f32 v92, v92, s65, v65
	v_med3_f32 v98, v98, s65, v65
	v_med3_f32 v100, v100, s65, v65
	v_med3_f32 v106, v106, s65, v65
	v_med3_f32 v108, v108, s65, v65
	v_med3_f32 v114, v114, s65, v65
	v_med3_f32 v116, v116, s65, v65
	v_cvt_pk_fp8_f32 v14, v121, v123
	v_cvt_pk_fp8_f32 v15, v129, v131
	v_cvt_pk_fp8_f32 v16, v137, v139
	v_cvt_pk_fp8_f32 v17, v145, v147
	s_waitcnt lgkmcnt(1)
	v_mul_f32_e32 v146, 0x43800000, v148
	v_mul_f32_e32 v148, 0x43800000, v149
	s_waitcnt lgkmcnt(0)
	v_mul_f32_e32 v149, 0x43800000, v150
	v_med3_f32 v93, v93, s65, v65
	v_med3_f32 v95, v95, s65, v65
	v_med3_f32 v101, v101, s65, v65
	v_med3_f32 v103, v103, s65, v65
	v_med3_f32 v109, v109, s65, v65
	v_med3_f32 v111, v111, s65, v65
	v_med3_f32 v117, v117, s65, v65
	v_med3_f32 v118, v118, s65, v65
	v_cvt_pk_fp8_f32 v2, v90, v92 op_sel:[0,0,1]
	v_cvt_pk_fp8_f32 v3, v98, v100 op_sel:[0,0,1]
	v_cvt_pk_fp8_f32 v4, v106, v108 op_sel:[0,0,1]
	v_cvt_pk_fp8_f32 v5, v114, v116 op_sel:[0,0,1]
	v_mul_f32_e32 v125, 0x43800000, v125
	v_mul_f32_e32 v127, 0x43800000, v127
	v_mul_f32_e32 v133, 0x43800000, v133
	v_mul_f32_e32 v135, 0x43800000, v135
	v_mul_f32_e32 v141, 0x43800000, v141
	v_mul_f32_e32 v143, 0x43800000, v143
	v_mul_f32_e32 v150, 0x43800000, v151
	v_med3_f32 v122, v122, s65, v65
	v_med3_f32 v124, v124, s65, v65
	v_med3_f32 v130, v130, s65, v65
	v_med3_f32 v132, v132, s65, v65
	v_med3_f32 v138, v138, s65, v65
	v_med3_f32 v140, v140, s65, v65
	v_med3_f32 v146, v146, s65, v65
	v_med3_f32 v149, v149, s65, v65
	v_cvt_pk_fp8_f32 v6, v93, v95 op_sel:[0,0,1]
	v_cvt_pk_fp8_f32 v7, v101, v103 op_sel:[0,0,1]
	v_cvt_pk_fp8_f32 v8, v109, v111 op_sel:[0,0,1]
	v_cvt_pk_fp8_f32 v9, v117, v118 op_sel:[0,0,1]
	v_med3_f32 v125, v125, s65, v65
	v_med3_f32 v127, v127, s65, v65
	v_med3_f32 v133, v133, s65, v65
	v_med3_f32 v135, v135, s65, v65
	v_med3_f32 v141, v141, s65, v65
	v_med3_f32 v143, v143, s65, v65
	v_med3_f32 v148, v148, s65, v65
	v_med3_f32 v150, v150, s65, v65
	v_cvt_pk_fp8_f32 v10, v122, v124 op_sel:[0,0,1]
	v_cvt_pk_fp8_f32 v11, v130, v132 op_sel:[0,0,1]
	v_cvt_pk_fp8_f32 v12, v138, v140 op_sel:[0,0,1]
	v_cvt_pk_fp8_f32 v13, v146, v149 op_sel:[0,0,1]
	v_cvt_pk_fp8_f32 v14, v125, v127 op_sel:[0,0,1]
	v_cvt_pk_fp8_f32 v15, v133, v135 op_sel:[0,0,1]
	v_cvt_pk_fp8_f32 v16, v141, v143 op_sel:[0,0,1]
	v_cvt_pk_fp8_f32 v17, v148, v150 op_sel:[0,0,1]
	global_store_dwordx4 v[38:39], v[2:5], off nt
	global_store_dwordx4 v[36:37], v[6:9], off nt
	global_store_dwordx4 v[34:35], v[10:13], off nt
	global_store_dwordx4 v[32:33], v[14:17], off nt
	v_add_u32_e32 v86, s3, v86
	s_waitcnt lgkmcnt(0)
	v_cmp_lt_i32_e64 s[0:1], s66, v86
	s_or_b64 s[14:15], s[0:1], s[14:15]
	v_add_u32_e32 v30, s67, v30
	s_andn2_b64 exec, exec, s[14:15]
	s_cbranch_execnz .LBB0_14
	s_branch .LBB0_7
.LBB0_15:
	s_cmp_ge_u32 s99, 2
	s_cbranch_scc1 .Ltr_fwd1
	v_lshlrev_b32_e32 v67, 2, v0
	v_and_b32_e32 v71, 60, v67
	v_bfe_u32 v93, v0, 4, 2
	v_lshlrev_b32_e32 v1, 2, v71
	v_mul_u32_u24_e32 v2, 0x104, v93
	v_add3_u32 v73, v31, v1, v2
	v_lshlrev_b32_e32 v1, 3, v0
	v_and_b32_e32 v2, 56, v1
	v_mul_u32_u24_e32 v3, 0x104, v2
	v_lshlrev_b32_e32 v4, 2, v66
	s_movk_i32 s0, 0x400
	v_mov_b32_e32 v77, 0
	v_add3_u32 v88, v31, v3, v4
	v_or_b32_e32 v89, 32, v66
	v_or_b32_e32 v90, 40, v66
	v_or_b32_e32 v91, 48, v66
	v_or_b32_e32 v92, 56, v66
	v_cmp_gt_i32_e64 s[6:7], s0, v69
	v_lshlrev_b32_e32 v76, 1, v2
	v_lshlrev_b32_e32 v94, 6, v186
	s_cmp_eq_u32 s99, 0
	s_cselect_b64 vcc, s[6:7], 0
	s_and_saveexec_b64 s[0:1], vcc
	s_cbranch_execz .LBB0_50
	v_lshl_add_u64 v[2:3], s[58:59], 0, v[76:77]
	s_mov_b64 s[8:9], 0x3da00000
	v_lshl_add_u64 v[82:83], v[2:3], 0, s[8:9]
	v_lshl_or_b32 v77, s96, 9, v94
	s_lshl_b32 s14, s3, 6
	s_mov_b64 s[8:9], 0
	s_movk_i32 s15, 0x800
	s_movk_i32 s16, 0x3ff
	v_mov_b32_e32 v95, v69
	s_branch .LBB0_18

.LBB0_1568:
	s_and_b64 vcc, exec, s[0:1]
	s_cbranch_vccz .LBB0_1579
	s_cmpk_lt_i32 s96, 64
	s_cbranch_scc1 .LBB0_1579
	s_cmpk_lt_i32 s96, 80
	s_cbranch_scc1 .Lrec_spare_a
	s_cmpk_lt_i32 s96, 230
	s_cbranch_scc1 .Lrec_conv
	v_writelane_b32 v237, s2, 0
	v_writelane_b32 v237, s96, 1
	v_writelane_b32 v237, s8, 2
	v_writelane_b32 v237, s9, 3
	s_sub_i32 s96, s96, 230
	s_movk_i32 s2, 26
	s_mov_b32 s99, 2
	s_branch .Lrec_spare_go
.Lrec_spare_a:
	v_writelane_b32 v237, s2, 0
	v_writelane_b32 v237, s96, 1
	v_writelane_b32 v237, s8, 2
	v_writelane_b32 v237, s9, 3
	s_sub_i32 s96, s96, 64
	s_movk_i32 s2, 16
	s_mov_b32 s99, 3
.Lrec_spare_go:
	s_mov_b32 s98, 2
	s_mov_b32 s100, 3
	s_waitcnt vmcnt(0) lgkmcnt(0)
	s_branch .Ltr_bwd3
